# diff-attn pair loop bookkeeping diet: 4-slot V ring with XOR-toggled slot offsets, running DMA source offsets, incremental V read addresses, M0 writes hoisted (no s_nop), on top of the QK/PV reschedul
# speedup vs baseline: 1.0037x; 1.0037x over previous
.LBB0_373:
	s_and_b32 s5, s19, 7
	s_mov_b32 s44, 0
	s_lshl_b64 s[10:11], s[44:45], 1
	s_add_u32 s4, s0, s10
	s_addc_u32 s22, s3, s11
	s_lshl_b32 s6, s19, 4
	s_and_b32 s6, s6, 0xffffff80
	s_or_b32 s20, s6, s80
	s_lshl_b32 s21, s5, 7
	s_lshl_b32 s6, s5, 8
	v_mov_b32_e32 v2, v175
	s_add_u32 s6, s4, s6
	s_addc_u32 s7, s22, 0
	v_ashrrev_i32_e32 v1, 4, v2
	s_add_u32 s6, s6, s39
	v_lshlrev_b32_e32 v4, 3, v1
	v_and_b32_e32 v0, 15, v2
	s_addc_u32 s7, s7, 0
	v_ashrrev_i32_e32 v5, 31, v4
	v_or_b32_e32 v8, s20, v0
	v_lshl_add_u64 v[4:5], v[4:5], 1, s[6:7]
	v_mad_i64_i32 v[6:7], s[6:7], v8, s65, v[4:5]
	global_load_dwordx4 v[120:123], v[6:7], off
	global_load_dwordx4 v[116:119], v[6:7], off offset:64
	v_or_b32_e32 v6, 16, v8
	v_mad_i64_i32 v[4:5], s[6:7], v6, s65, v[4:5]
	global_load_dwordx4 v[124:127], v[4:5], off
	global_load_dwordx4 v[128:131], v[4:5], off offset:64
	s_lshl_b32 s5, s5, 21
	v_mov_b32_e32 v84, v176
	s_add_u32 s40, s15, s5
	s_addc_u32 s23, s16, 0
	v_readfirstlane_b32 s5, v84
	v_and_b32_e32 v4, 63, v84
	s_ashr_i32 s25, s5, 6
	v_bfe_u32 v85, v84, 4, 2
	s_and_b32 s5, s22, 0xffff
	s_lshl_b32 s22, s25, 1
	s_lshl_b32 s26, s25, 3
	v_lshl_or_b32 v8, s25, 7, v4
	v_bitop3_b32 v7, s26, v84, v85 bitop3:0x36
	v_ashrrev_i32_e32 v8, 3, v8
	s_or_b32 s22, s22, 1
	s_or_b32 s24, s21, 0x400
	v_and_b32_e32 v5, 7, v84
	v_or_b32_e32 v6, s26, v85
	v_lshlrev_b32_e32 v7, 3, v7
	v_lshlrev_b32_e32 v9, 7, v8
	v_lshrrev_b32_e32 v8, 1, v8
	s_lshl_b32 s26, s22, 2
	v_lshl_or_b32 v4, s22, 6, v4
	s_and_b32 s41, s23, 0xffff
	s_lshl_b32 s22, s25, 11
	v_and_b32_e32 v7, 0x78, v7
	v_bitop3_b32 v8, v8, v5, 1 bitop3:0x6c
	v_mul_lo_u32 v6, v6, s48
	v_ashrrev_i32_e32 v4, 3, v4
	s_cmp_lg_u32 0, -1
	v_lshl_or_b32 v183, v8, 4, v9
	v_or3_b32 v6, v7, v6, s24
	v_bitop3_b32 v7, s26, v84, v85 bitop3:0x36
	v_lshlrev_b32_e32 v8, 7, v4
	v_bfe_u32 v4, v4, 1, 1
	s_cselect_b32 s44, 0, 0
	v_lshlrev_b32_e32 v184, 1, v6
	v_or_b32_e32 v6, s26, v85
	v_lshlrev_b32_e32 v7, 3, v7
	v_bitop3_b32 v4, v4, v5, 6 bitop3:0x36
	s_add_i32 s26, s44, 0x10000
	v_and_b32_e32 v7, 0x78, v7
	v_lshl_or_b32 v185, v4, 4, v8
	v_mul_lo_u32 v4, v6, s48
	s_add_i32 m0, s26, s22
	s_add_i32 s23, s44, s22
	s_mov_b32 s6, s42
	s_mov_b32 s7, s43
	v_or3_b32 v4, v7, v4, s24
	v_mov_b32 v40, 0x22222222
	v_mov_b32 v41, 0x22222222
	v_mov_b32 v42, 0x22222222
	v_mov_b32 v43, 0x22222222
	buffer_load_dwordx4 v183, s[40:43], 0 offen lds
	s_mov_b32 m0, s23
	s_add_i32 s24, s23, 0x4000
	buffer_load_dwordx4 v184, s[4:7], 0 offen lds
	s_mov_b32 m0, s24
	s_mov_b32 s29, 0xc0000
	s_or_b32 s25, s22, 0x400
	buffer_load_dwordx4 v184, s[4:7], s29 offen lds
	s_add_i32 m0, s26, s25
	s_add_i32 s26, s23, 0x400
	v_lshlrev_b32_e32 v186, 1, v4
	buffer_load_dwordx4 v185, s[40:43], 0 offen lds
	s_mov_b32 m0, s26
	s_add_i32 s27, s23, 0x4400
	buffer_load_dwordx4 v186, s[4:7], 0 offen lds
	s_mov_b32 m0, s27
	s_add_i32 s34, s44, 0x14000
	buffer_load_dwordx4 v186, s[4:7], s29 offen lds
	s_waitcnt vmcnt(0)
	s_barrier
	s_add_i32 m0, s34, s22
	s_add_i32 s29, s23, 0x8000
	buffer_load_dwordx4 v183, s[40:43], s91 offen lds
	s_mov_b32 m0, s29
	s_mov_b32 s35, 0x180000
	s_add_i32 s31, s23, 0xc000
	buffer_load_dwordx4 v184, s[4:7], s35 offen lds
	s_mov_b32 m0, s31
	s_mov_b32 s36, 0x240000
	buffer_load_dwordx4 v184, s[4:7], s36 offen lds
	s_add_i32 m0, s34, s25
	s_add_i32 s34, s23, 0x8400
	buffer_load_dwordx4 v185, s[40:43], s91 offen lds
	s_mov_b32 m0, s34
	v_and_b32_e32 v86, 15, v84
	buffer_load_dwordx4 v186, s[4:7], s35 offen lds
	s_add_i32 s35, s23, 0xc400
	s_mov_b32 m0, s35
	v_bitop3_b32 v4, v85, v86, s81 bitop3:0x36
	buffer_load_dwordx4 v186, s[4:7], s36 offen lds
	v_lshlrev_b32_e32 v4, 4, v4
	v_lshl_add_u32 v8, v86, 8, s44
	v_add_u32_e32 v181, v8, v4
	ds_read_b128 v[4:7], v181
	v_or_b32_e32 v9, s81, v85
	v_bitop3_b32 v9, v9, v86, 4 bitop3:0x36
	v_lshlrev_b32_e32 v9, 4, v9
	v_add_u32_e32 v182, v8, v9
	ds_read_b128 v[8:11], v181 offset:4096
	s_waitcnt vmcnt(15) lgkmcnt(0)
	v_mfma_f32_16x16x32_bf16 v[12:15], v[4:7], v[120:123], v[36:39]
	ds_read_b128 v[16:19], v182
	ds_read_b128 v[20:23], v182 offset:4096
	v_cmp_gt_u32_e32 vcc, 8, v86
	s_mov_b32 s36, 3
	s_waitcnt vmcnt(13)
	v_mfma_f32_16x16x32_bf16 v[4:7], v[4:7], v[124:127], v[36:39]
	s_mov_b32 s37, 2
	s_mov_b32 s50, 0
	v_lshl_add_u32 v180, v86, 7, s44
	s_waitcnt lgkmcnt(1)
	v_mfma_f32_16x16x32_bf16 v[12:15], v[16:19], v[116:119], v[12:15]
	s_mov_b32 s44, 0x300000
	s_waitcnt vmcnt(12)
	v_mfma_f32_16x16x32_bf16 v[16:19], v[16:19], v[128:131], v[4:7]
	v_mfma_f32_16x16x32_bf16 v[4:7], v[8:11], v[120:123], v[36:39]
	s_waitcnt lgkmcnt(0)
	v_mfma_f32_16x16x32_bf16 v[24:27], v[20:23], v[116:119], v[4:7]
	v_mfma_f32_16x16x32_bf16 v[4:7], v[8:11], v[124:127], v[36:39]
	v_lshlrev_b32_e32 v11, 1, v85
	v_mfma_f32_16x16x32_bf16 v[6:9], v[20:23], v[128:131], v[4:7]
	ds_read_b128 v[20:23], v181 offset:8192
	ds_read_b128 v[28:31], v181 offset:12288
	ds_read_b128 v[44:47], v182 offset:8192
	ds_read_b128 v[48:51], v182 offset:12288
	s_nop 1
	v_bfe_u32 v4, v84, 1, 1
	v_cndmask_b32_e64 v5, 6, 0, vcc
	v_or_b32_e32 v10, v5, v4
	v_bitop3_b32 v4, v5, v11, v4 bitop3:0x36
	s_waitcnt lgkmcnt(3)
	v_mfma_f32_16x16x32_bf16 v[32:35], v[20:23], v[120:123], v[36:39]
	v_lshlrev_b32_e32 v178, 4, v4
	v_exp_f32_e32 v4, v12
	v_exp_f32_e32 v5, v13
	v_mfma_f32_16x16x32_bf16 v[20:23], v[20:23], v[124:127], v[36:39]
	v_exp_f32_e32 v12, v16
	v_exp_f32_e32 v13, v17
	v_bitop3_b32 v84, v11, v10, 1 bitop3:0x36
	s_waitcnt lgkmcnt(1)
	v_mfma_f32_16x16x32_bf16 v[32:35], v[44:47], v[116:119], v[32:35]
	v_exp_f32_e32 v10, v14
	v_cvt_pk_fp8_f32 v12, v12, v13
	v_exp_f32_e32 v13, v6
	v_mfma_f32_16x16x32_bf16 v[20:23], v[44:47], v[128:131], v[20:23]
	v_exp_f32_e32 v6, v7
	v_exp_f32_e32 v11, v15
	v_cvt_pk_fp8_f32 v4, v4, v5
	v_mfma_f32_16x16x32_bf16 v[44:47], v[28:31], v[120:123], v[36:39]
	v_exp_f32_e32 v14, v18
	v_exp_f32_e32 v15, v19
	v_exp_f32_e32 v7, v8
	v_mfma_f32_16x16x32_bf16 v[28:31], v[28:31], v[124:127], v[36:39]
	v_exp_f32_e32 v8, v9
	v_cvt_pk_fp8_f32 v13, v13, v6
	v_exp_f32_e32 v5, v24
	s_waitcnt lgkmcnt(0)
	v_mfma_f32_16x16x32_bf16 v[44:47], v[48:51], v[116:119], v[44:47]
	v_exp_f32_e32 v16, v25
	v_cvt_pk_fp8_f32 v4, v10, v11 op_sel:[0,0,1]
	v_cvt_pk_fp8_f32 v12, v14, v15 op_sel:[0,0,1]
	v_mfma_f32_16x16x32_bf16 v[28:31], v[48:51], v[128:131], v[28:31]
	ds_read_b128 v[48:51], v181 offset:16384
	ds_read_b128 v[52:55], v181 offset:20480
	ds_read_b128 v[60:63], v182 offset:16384
	ds_read_b128 v[64:67], v182 offset:20480
	v_cvt_pk_fp8_f32 v13, v7, v8 op_sel:[0,0,1]
	s_waitcnt lgkmcnt(3)
	v_mfma_f32_16x16x32_bf16 v[56:59], v[48:51], v[120:123], v[36:39]
	v_exp_f32_e32 v6, v32
	v_exp_f32_e32 v7, v33
	v_exp_f32_e32 v14, v20
	v_mfma_f32_16x16x32_bf16 v[48:51], v[48:51], v[124:127], v[36:39]
	v_exp_f32_e32 v10, v21
	v_exp_f32_e32 v17, v26
	v_exp_f32_e32 v18, v27
	s_waitcnt lgkmcnt(1)
	v_mfma_f32_16x16x32_bf16 v[56:59], v[60:63], v[116:119], v[56:59]
	v_cvt_pk_fp8_f32 v5, v5, v16
	v_cvt_pk_fp8_f32 v6, v6, v7
	v_cvt_pk_fp8_f32 v14, v14, v10
	v_mfma_f32_16x16x32_bf16 v[48:51], v[60:63], v[128:131], v[48:51]
	v_exp_f32_e32 v7, v44
	v_exp_f32_e32 v10, v45
	v_cvt_pk_fp8_f32 v5, v17, v18 op_sel:[0,0,1]
	v_mfma_f32_16x16x32_bf16 v[60:63], v[52:55], v[120:123], v[36:39]
	v_exp_f32_e32 v8, v34
	v_exp_f32_e32 v9, v35
	v_exp_f32_e32 v11, v22
	v_mfma_f32_16x16x32_bf16 v[52:55], v[52:55], v[124:127], v[36:39]
	v_exp_f32_e32 v16, v23
	v_exp_f32_e32 v17, v46
	v_exp_f32_e32 v18, v47
	s_waitcnt lgkmcnt(0)
	v_mfma_f32_16x16x32_bf16 v[60:63], v[64:67], v[116:119], v[60:63]
	v_exp_f32_e32 v15, v28
	v_exp_f32_e32 v19, v29
	v_cvt_pk_fp8_f32 v7, v7, v10
	v_mfma_f32_16x16x32_bf16 v[52:55], v[64:67], v[128:131], v[52:55]
	ds_read_b128 v[64:67], v181 offset:24576
	ds_read_b128 v[68:71], v181 offset:28672
	ds_read_b128 v[76:79], v182 offset:24576
	ds_read_b128 v[80:83], v182 offset:28672
	v_exp_f32_e32 v10, v30
	s_waitcnt lgkmcnt(3)
	v_mfma_f32_16x16x32_bf16 v[72:75], v[64:67], v[120:123], v[36:39]
	v_exp_f32_e32 v20, v31
	v_cvt_pk_fp8_f32 v15, v15, v19
	v_cvt_pk_fp8_f32 v6, v8, v9 op_sel:[0,0,1]
	v_mfma_f32_16x16x32_bf16 v[64:67], v[64:67], v[124:127], v[36:39]
	v_cvt_pk_fp8_f32 v14, v11, v16 op_sel:[0,0,1]
	v_cvt_pk_fp8_f32 v7, v17, v18 op_sel:[0,0,1]
	v_exp_f32_e32 v8, v56
	v_exp_f32_e32 v9, v57
	v_exp_f32_e32 v16, v48
	v_exp_f32_e32 v17, v49
	s_waitcnt lgkmcnt(1)
	v_mfma_f32_16x16x32_bf16 v[72:75], v[76:79], v[116:119], v[72:75]
	v_cvt_pk_fp8_f32 v15, v10, v20 op_sel:[0,0,1]
	v_exp_f32_e32 v10, v58
	v_exp_f32_e32 v11, v59
	v_mfma_f32_16x16x32_bf16 v[64:67], v[76:79], v[128:131], v[64:67]
	v_cvt_pk_fp8_f32 v8, v8, v9
	v_exp_f32_e32 v18, v50
	v_exp_f32_e32 v19, v51
	v_mfma_f32_16x16x32_bf16 v[76:79], v[68:71], v[120:123], v[36:39]
	v_cvt_pk_fp8_f32 v16, v16, v17
	v_exp_f32_e32 v9, v60
	v_exp_f32_e32 v20, v61
	v_mfma_f32_16x16x32_bf16 v[68:71], v[68:71], v[124:127], v[36:39]
	v_exp_f32_e32 v17, v52
	v_exp_f32_e32 v23, v53
	v_cvt_pk_fp8_f32 v9, v9, v20
	s_waitcnt lgkmcnt(0)
	v_mfma_f32_16x16x32_bf16 v[76:79], v[80:83], v[116:119], v[76:79]
	v_exp_f32_e32 v20, v54
	v_exp_f32_e32 v24, v55
	v_cvt_pk_fp8_f32 v17, v17, v23
	v_mfma_f32_16x16x32_bf16 v[68:71], v[80:83], v[128:131], v[68:71]
	v_cvt_pk_fp8_f32 v8, v10, v11 op_sel:[0,0,1]
	v_cvt_pk_fp8_f32 v16, v18, v19 op_sel:[0,0,1]
	v_exp_f32_e32 v10, v72
	v_exp_f32_e32 v11, v73
	v_exp_f32_e32 v18, v64
	v_exp_f32_e32 v19, v65
	v_exp_f32_e32 v21, v62
	v_exp_f32_e32 v22, v63
	v_cvt_pk_fp8_f32 v17, v20, v24 op_sel:[0,0,1]
	v_cvt_pk_fp8_f32 v10, v10, v11
	v_cvt_pk_fp8_f32 v18, v18, v19
	v_exp_f32_e32 v11, v76
	v_exp_f32_e32 v24, v77
	v_exp_f32_e32 v19, v68
	v_exp_f32_e32 v27, v69
	v_cvt_pk_fp8_f32 v9, v21, v22 op_sel:[0,0,1]
	v_exp_f32_e32 v20, v74
	v_exp_f32_e32 v21, v75
	v_exp_f32_e32 v22, v66
	v_exp_f32_e32 v23, v67
	v_exp_f32_e32 v25, v78
	v_exp_f32_e32 v26, v79
	v_cvt_pk_fp8_f32 v11, v11, v24
	v_exp_f32_e32 v24, v70
	v_exp_f32_e32 v28, v71
	v_cvt_pk_fp8_f32 v19, v19, v27
	v_cvt_pk_fp8_f32 v10, v20, v21 op_sel:[0,0,1]
	v_cvt_pk_fp8_f32 v18, v22, v23 op_sel:[0,0,1]
	v_cvt_pk_fp8_f32 v11, v25, v26 op_sel:[0,0,1]
	v_cvt_pk_fp8_f32 v19, v24, v28 op_sel:[0,0,1]
	v_mov_b32_e32 v44, 0
	v_lshlrev_b32_e32 v179, 4, v84
	v_mov_b32_e32 v45, v44
	v_mov_b32_e32 v46, v44
	v_mov_b32_e32 v47, v44
	v_mov_b32_e32 v68, v44
	v_mov_b32_e32 v69, v44
	v_mov_b32_e32 v70, v44
	v_mov_b32_e32 v71, v44
	v_mov_b32_e32 v48, v44
	v_mov_b32_e32 v49, v44
	v_mov_b32_e32 v50, v44
	v_mov_b32_e32 v51, v44
	v_mov_b32_e32 v76, v44
	v_mov_b32_e32 v77, v44
	v_mov_b32_e32 v78, v44
	v_mov_b32_e32 v79, v44
	v_mov_b32_e32 v52, v44
	v_mov_b32_e32 v53, v44
	v_mov_b32_e32 v54, v44
	v_mov_b32_e32 v55, v44
	v_mov_b32_e32 v84, v44
	v_mov_b32_e32 v85, v44
	v_mov_b32_e32 v86, v44
	v_mov_b32_e32 v87, v44
	v_mov_b32_e32 v56, v44
	v_mov_b32_e32 v57, v44
	v_mov_b32_e32 v58, v44
	v_mov_b32_e32 v59, v44
	v_mov_b32_e32 v92, v44
	v_mov_b32_e32 v93, v44
	v_mov_b32_e32 v94, v44
	v_mov_b32_e32 v95, v44
	v_mov_b32_e32 v60, v44
	v_mov_b32_e32 v61, v44
	v_mov_b32_e32 v62, v44
	v_mov_b32_e32 v63, v44
	v_mov_b32_e32 v96, v44
	v_mov_b32_e32 v97, v44
	v_mov_b32_e32 v98, v44
	v_mov_b32_e32 v99, v44
	v_mov_b32_e32 v64, v44
	v_mov_b32_e32 v65, v44
	v_mov_b32_e32 v66, v44
	v_mov_b32_e32 v67, v44
	v_mov_b32_e32 v100, v44
	v_mov_b32_e32 v101, v44
	v_mov_b32_e32 v102, v44
	v_mov_b32_e32 v103, v44
	v_mov_b32_e32 v72, v44
	v_mov_b32_e32 v73, v44
	v_mov_b32_e32 v74, v44
	v_mov_b32_e32 v75, v44
	v_mov_b32_e32 v104, v44
	v_mov_b32_e32 v105, v44
	v_mov_b32_e32 v106, v44
	v_mov_b32_e32 v107, v44
	v_mov_b32_e32 v80, v44
	v_mov_b32_e32 v81, v44
	v_mov_b32_e32 v82, v44
	v_mov_b32_e32 v83, v44
	v_mov_b32_e32 v108, v44
	v_mov_b32_e32 v109, v44
	v_mov_b32_e32 v110, v44
	v_mov_b32_e32 v111, v44
	v_mov_b32_e32 v88, v44
	v_mov_b32_e32 v89, v44
	v_mov_b32_e32 v90, v44
	v_mov_b32_e32 v91, v44
	v_mov_b32_e32 v112, v44
	v_mov_b32_e32 v113, v44
	v_mov_b32_e32 v114, v44
	v_mov_b32_e32 v115, v44
	s_add_i32 s53, s22, 0x18000
	s_mov_b32 s51, 0xffff4000
	s_mov_b32 s47, 0x8000
	s_mov_b32 s46, 0xc000
	s_mov_b32 s6, s42
	s_mov_b32 s7, s43
	v_add_u32_e32 v187, v180, v178
	v_add_u32_e32 v206, v180, v179
	v_add_u32_e32 v187, 0x1c000, v187
	v_add_u32_e32 v206, 0x1c000, v206
.LBB0_374:
	s_waitcnt vmcnt(0)
	s_barrier
	ds_read_b128 v[132:135], v181 offset:32768
	ds_read_b128 v[136:139], v181 offset:36864
	ds_read_b128 v[140:143], v182 offset:32768
	ds_read_b128 v[144:147], v182 offset:36864
	ds_read_b128 v[188:191], v181 offset:40960
	ds_read_b128 v[192:195], v181 offset:45056
	ds_read_b128 v[222:225], v182 offset:40960
	ds_read_b128 v[226:229], v182 offset:45056
	s_mov_b32 m0, s53
	s_add_i32 s54, s44, 0xc0000
	buffer_load_dwordx4 v183, s[40:43], s47 offen lds
	s_mov_b32 m0, s23
	s_nop 0
	buffer_load_dwordx4 v184, s[4:7], s44 offen lds
	s_mov_b32 m0, s24
	s_waitcnt lgkmcnt(6)
	v_mfma_f32_16x16x32_bf16 v[28:31], v[132:135], v[120:123], v[36:39]
	v_mfma_f32_16x16x32_bf16 v[230:233], v[132:135], v[124:127], v[36:39]
	v_mfma_f32_16x16x32_bf16 v[234:237], v[136:139], v[120:123], v[36:39]
	v_mfma_f32_16x16x32_bf16 v[238:241], v[136:139], v[124:127], v[36:39]
	s_waitcnt lgkmcnt(4)
	v_mfma_f32_16x16x32_bf16 v[28:31], v[140:143], v[116:119], v[28:31]
	v_mfma_f32_16x16x32_bf16 v[230:233], v[140:143], v[128:131], v[230:233]
	v_mfma_f32_16x16x32_bf16 v[234:237], v[144:147], v[116:119], v[234:237]
	v_mfma_f32_16x16x32_bf16 v[238:241], v[144:147], v[128:131], v[238:241]
	ds_read_b128 v[132:135], v181 offset:49152
	ds_read_b128 v[136:139], v181 offset:53248
	ds_read_b128 v[140:143], v182 offset:49152
	ds_read_b128 v[144:147], v182 offset:53248
	buffer_load_dwordx4 v184, s[4:7], s54 offen lds
	s_add_i32 m0, s53, 0x400
	s_waitcnt lgkmcnt(6)
	v_mfma_f32_16x16x32_bf16 v[168:171], v[188:191], v[120:123], v[36:39]
	v_mfma_f32_16x16x32_bf16 v[164:167], v[188:191], v[124:127], v[36:39]
	v_mfma_f32_16x16x32_bf16 v[160:163], v[192:195], v[120:123], v[36:39]
	v_mfma_f32_16x16x32_bf16 v[156:159], v[192:195], v[124:127], v[36:39]
	s_waitcnt lgkmcnt(4)
	v_mfma_f32_16x16x32_bf16 v[168:171], v[222:225], v[116:119], v[168:171]
	v_mfma_f32_16x16x32_bf16 v[164:167], v[222:225], v[128:131], v[164:167]
	v_mfma_f32_16x16x32_bf16 v[160:163], v[226:229], v[116:119], v[160:163]
	v_mfma_f32_16x16x32_bf16 v[156:159], v[226:229], v[128:131], v[156:159]
	ds_read_b128 v[188:191], v181 offset:57344
	ds_read_b128 v[192:195], v181 offset:61440
	ds_read_b128 v[222:225], v182 offset:57344
	ds_read_b128 v[226:229], v182 offset:61440
	buffer_load_dwordx4 v185, s[40:43], s47 offen lds
	s_mov_b32 m0, s26
	s_waitcnt lgkmcnt(6)
	v_mfma_f32_16x16x32_bf16 v[24:27], v[132:135], v[120:123], v[36:39]
	v_mfma_f32_16x16x32_bf16 v[32:35], v[132:135], v[124:127], v[36:39]
	v_mfma_f32_16x16x32_bf16 v[152:155], v[136:139], v[120:123], v[36:39]
	v_mfma_f32_16x16x32_bf16 v[148:151], v[136:139], v[124:127], v[36:39]
	s_waitcnt lgkmcnt(4)
	v_mfma_f32_16x16x32_bf16 v[24:27], v[140:143], v[116:119], v[24:27]
	v_mfma_f32_16x16x32_bf16 v[32:35], v[140:143], v[128:131], v[32:35]
	v_mfma_f32_16x16x32_bf16 v[152:155], v[144:147], v[116:119], v[152:155]
	v_mfma_f32_16x16x32_bf16 v[148:151], v[144:147], v[128:131], v[148:151]
	buffer_load_dwordx4 v186, s[4:7], s44 offen lds
	s_mov_b32 m0, s27
	s_waitcnt lgkmcnt(2)
	v_mfma_f32_16x16x32_bf16 v[144:147], v[188:191], v[120:123], v[36:39]
	v_mfma_f32_16x16x32_bf16 v[140:143], v[188:191], v[124:127], v[36:39]
	v_mfma_f32_16x16x32_bf16 v[136:139], v[192:195], v[120:123], v[36:39]
	v_mfma_f32_16x16x32_bf16 v[132:135], v[192:195], v[124:127], v[36:39]
	buffer_load_dwordx4 v186, s[4:7], s54 offen lds
	s_waitcnt lgkmcnt(0)
	v_mfma_f32_16x16x32_bf16 v[144:147], v[222:225], v[116:119], v[144:147]
	v_mfma_f32_16x16x32_bf16 v[140:143], v[222:225], v[128:131], v[140:143]
	v_mfma_f32_16x16x32_bf16 v[136:139], v[226:229], v[116:119], v[136:139]
	v_mfma_f32_16x16x32_bf16 v[132:135], v[226:229], v[128:131], v[132:135]
	v_add_u32_e32 v187, s51, v187
	v_add_u32_e32 v206, s51, v206
	v_exp_f32_e32 v20, v28
	v_exp_f32_e32 v21, v29
	v_exp_f32_e32 v22, v30
	v_exp_f32_e32 v23, v31
	v_exp_f32_e32 v28, v230
	v_cvt_pk_fp8_f32 v20, v20, v21
	v_exp_f32_e32 v21, v231
	ds_read_b128 v[188:191], v187
	ds_read_b128 v[192:195], v206
	v_mfma_f32_16x16x128_f8f6f4 v[112:115], v[4:11], v[40:43], v[112:115] blgp:4
	ds_read_b128 v[222:225], v187 offset:2048
	ds_read_b128 v[226:229], v206 offset:2048
	v_cvt_pk_fp8_f32 v20, v22, v23 op_sel:[0,0,1]
	v_exp_f32_e32 v22, v232
	v_mfma_f32_16x16x128_f8f6f4 v[88:91], v[12:19], v[40:43], v[88:91] blgp:4
	v_exp_f32_e32 v23, v233
	v_cvt_pk_fp8_f32 v28, v28, v21
	s_waitcnt lgkmcnt(2)
	v_mfma_f32_16x16x128_f8f6f4 v[108:111], v[4:11], v[188:195], v[108:111]
	v_cvt_pk_fp8_f32 v28, v22, v23 op_sel:[0,0,1]
	v_exp_f32_e32 v21, v234
	v_exp_f32_e32 v22, v235
	v_exp_f32_e32 v29, v238
	v_mfma_f32_16x16x128_f8f6f4 v[80:83], v[12:19], v[188:195], v[80:83]
	v_exp_f32_e32 v31, v239
	ds_read_b128 v[188:191], v187 offset:4096
	ds_read_b128 v[192:195], v206 offset:4096
	v_exp_f32_e32 v23, v236
	v_exp_f32_e32 v30, v237
	v_cvt_pk_fp8_f32 v21, v21, v22
	v_exp_f32_e32 v22, v240
	v_exp_f32_e32 v207, v241
	v_cvt_pk_fp8_f32 v29, v29, v31
	v_cvt_pk_fp8_f32 v21, v23, v30 op_sel:[0,0,1]
	s_waitcnt lgkmcnt(2)
	v_mfma_f32_16x16x128_f8f6f4 v[104:107], v[4:11], v[222:229], v[104:107]
	v_cvt_pk_fp8_f32 v29, v22, v207 op_sel:[0,0,1]
	v_exp_f32_e32 v22, v168
	v_exp_f32_e32 v23, v169
	v_exp_f32_e32 v30, v164
	v_mfma_f32_16x16x128_f8f6f4 v[72:75], v[12:19], v[222:229], v[72:75]
	v_exp_f32_e32 v164, v165
	v_exp_f32_e32 v31, v170
	v_exp_f32_e32 v207, v171
	v_cvt_pk_fp8_f32 v22, v22, v23
	v_exp_f32_e32 v23, v166
	v_exp_f32_e32 v211, v167
	v_cvt_pk_fp8_f32 v30, v30, v164
	ds_read_b128 v[164:167], v187 offset:6144
	ds_read_b128 v[168:171], v206 offset:6144
	v_cvt_pk_fp8_f32 v22, v31, v207 op_sel:[0,0,1]
	s_waitcnt lgkmcnt(2)
	v_mfma_f32_16x16x128_f8f6f4 v[100:103], v[4:11], v[188:195], v[100:103]
	v_cvt_pk_fp8_f32 v30, v23, v211 op_sel:[0,0,1]
	v_exp_f32_e32 v23, v160
	v_exp_f32_e32 v160, v161
	v_exp_f32_e32 v31, v156
	v_mfma_f32_16x16x128_f8f6f4 v[64:67], v[12:19], v[188:195], v[64:67]
	v_exp_f32_e32 v156, v157
	v_exp_f32_e32 v188, v162
	v_exp_f32_e32 v189, v163
	v_cvt_pk_fp8_f32 v23, v23, v160
	v_exp_f32_e32 v190, v158
	v_exp_f32_e32 v191, v159
	v_cvt_pk_fp8_f32 v31, v31, v156
	ds_read_b128 v[156:159], v187 offset:8192
	ds_read_b128 v[160:163], v206 offset:8192
	v_cvt_pk_fp8_f32 v23, v188, v189 op_sel:[0,0,1]
	s_waitcnt lgkmcnt(2)
	v_mfma_f32_16x16x128_f8f6f4 v[96:99], v[4:11], v[164:171], v[96:99]
	v_cvt_pk_fp8_f32 v31, v190, v191 op_sel:[0,0,1]
	v_exp_f32_e32 v24, v24
	v_exp_f32_e32 v25, v25
	v_exp_f32_e32 v32, v32
	v_mfma_f32_16x16x128_f8f6f4 v[60:63], v[12:19], v[164:171], v[60:63]
	v_exp_f32_e32 v33, v33
	ds_read_b128 v[164:167], v187 offset:10240
	ds_read_b128 v[168:171], v206 offset:10240
	v_exp_f32_e32 v26, v26
	v_exp_f32_e32 v27, v27
	v_cvt_pk_fp8_f32 v24, v24, v25
	v_exp_f32_e32 v25, v34
	v_exp_f32_e32 v34, v35
	v_cvt_pk_fp8_f32 v32, v32, v33
	v_cvt_pk_fp8_f32 v24, v26, v27 op_sel:[0,0,1]
	s_waitcnt lgkmcnt(2)
	v_mfma_f32_16x16x128_f8f6f4 v[92:95], v[4:11], v[156:163], v[92:95]
	v_cvt_pk_fp8_f32 v32, v25, v34 op_sel:[0,0,1]
	v_exp_f32_e32 v25, v152
	v_exp_f32_e32 v26, v153
	v_exp_f32_e32 v33, v148
	v_mfma_f32_16x16x128_f8f6f4 v[56:59], v[12:19], v[156:163], v[56:59]
	v_exp_f32_e32 v35, v149
	v_exp_f32_e32 v27, v154
	v_exp_f32_e32 v34, v155
	v_cvt_pk_fp8_f32 v25, v25, v26
	v_exp_f32_e32 v26, v150
	v_exp_f32_e32 v156, v151
	ds_read_b128 v[148:151], v187 offset:12288
	ds_read_b128 v[152:155], v206 offset:12288
	v_cvt_pk_fp8_f32 v33, v33, v35
	v_cvt_pk_fp8_f32 v25, v27, v34 op_sel:[0,0,1]
	s_waitcnt lgkmcnt(2)
	v_mfma_f32_16x16x128_f8f6f4 v[84:87], v[4:11], v[164:171], v[84:87]
	v_cvt_pk_fp8_f32 v33, v26, v156 op_sel:[0,0,1]
	v_exp_f32_e32 v26, v144
	v_exp_f32_e32 v27, v145
	v_exp_f32_e32 v34, v140
	v_mfma_f32_16x16x128_f8f6f4 v[52:55], v[12:19], v[164:171], v[52:55]
	v_exp_f32_e32 v140, v141
	v_exp_f32_e32 v35, v146
	v_exp_f32_e32 v156, v147
	v_cvt_pk_fp8_f32 v26, v26, v27
	v_exp_f32_e32 v27, v142
	v_exp_f32_e32 v157, v143
	v_cvt_pk_fp8_f32 v34, v34, v140
	ds_read_b128 v[140:143], v187 offset:14336
	ds_read_b128 v[144:147], v206 offset:14336
	v_cvt_pk_fp8_f32 v26, v35, v156 op_sel:[0,0,1]
	s_waitcnt lgkmcnt(2)
	v_mfma_f32_16x16x128_f8f6f4 v[76:79], v[4:11], v[148:155], v[76:79]
	v_cvt_pk_fp8_f32 v34, v27, v157 op_sel:[0,0,1]
	v_mfma_f32_16x16x128_f8f6f4 v[48:51], v[12:19], v[148:155], v[48:51]
	s_waitcnt lgkmcnt(0)
	v_mfma_f32_16x16x128_f8f6f4 v[68:71], v[4:11], v[140:147], v[68:71]
	v_exp_f32_e32 v27, v136
	v_exp_f32_e32 v4, v137
	v_exp_f32_e32 v5, v138
	v_exp_f32_e32 v6, v139
	v_exp_f32_e32 v35, v132
	v_cvt_pk_fp8_f32 v27, v27, v4
	v_exp_f32_e32 v4, v133
	v_mfma_f32_16x16x128_f8f6f4 v[44:47], v[12:19], v[140:147], v[44:47]
	v_cvt_pk_fp8_f32 v27, v5, v6 op_sel:[0,0,1]
	v_exp_f32_e32 v5, v134
	v_exp_f32_e32 v6, v135
	v_cvt_pk_fp8_f32 v35, v35, v4
	v_cvt_pk_fp8_f32 v35, v5, v6 op_sel:[0,0,1]
	s_waitcnt vmcnt(0)
	s_barrier
	ds_read_b128 v[132:135], v181
	ds_read_b128 v[136:139], v181 offset:4096
	ds_read_b128 v[140:143], v182
	ds_read_b128 v[144:147], v182 offset:4096
	ds_read_b128 v[164:167], v181 offset:8192
	ds_read_b128 v[168:171], v181 offset:12288
	ds_read_b128 v[188:191], v182 offset:8192
	ds_read_b128 v[192:195], v182 offset:12288
	s_add_i32 m0, s53, 0x4000
	s_add_i32 s54, s44, 0x180000
	buffer_load_dwordx4 v183, s[40:43], s46 offen lds
	s_mov_b32 m0, s29
	s_add_i32 s55, s44, 0x240000
	buffer_load_dwordx4 v184, s[4:7], s54 offen lds
	s_mov_b32 m0, s31
	s_waitcnt lgkmcnt(6)
	v_mfma_f32_16x16x32_bf16 v[12:15], v[132:135], v[120:123], v[36:39]
	v_mfma_f32_16x16x32_bf16 v[222:225], v[132:135], v[124:127], v[36:39]
	v_mfma_f32_16x16x32_bf16 v[226:229], v[136:139], v[120:123], v[36:39]
	v_mfma_f32_16x16x32_bf16 v[230:233], v[136:139], v[124:127], v[36:39]
	s_waitcnt lgkmcnt(4)
	v_mfma_f32_16x16x32_bf16 v[12:15], v[140:143], v[116:119], v[12:15]
	v_mfma_f32_16x16x32_bf16 v[222:225], v[140:143], v[128:131], v[222:225]
	v_mfma_f32_16x16x32_bf16 v[226:229], v[144:147], v[116:119], v[226:229]
	v_mfma_f32_16x16x32_bf16 v[230:233], v[144:147], v[128:131], v[230:233]
	ds_read_b128 v[132:135], v181 offset:16384
	ds_read_b128 v[136:139], v181 offset:20480
	ds_read_b128 v[140:143], v182 offset:16384
	ds_read_b128 v[144:147], v182 offset:20480
	buffer_load_dwordx4 v184, s[4:7], s55 offen lds
	s_add_i32 m0, s53, 0x4400
	s_waitcnt lgkmcnt(6)
	v_mfma_f32_16x16x32_bf16 v[234:237], v[164:167], v[120:123], v[36:39]
	v_mfma_f32_16x16x32_bf16 v[238:241], v[164:167], v[124:127], v[36:39]
	v_mfma_f32_16x16x32_bf16 v[160:163], v[168:171], v[120:123], v[36:39]
	v_mfma_f32_16x16x32_bf16 v[156:159], v[168:171], v[124:127], v[36:39]
	s_waitcnt lgkmcnt(4)
	v_mfma_f32_16x16x32_bf16 v[234:237], v[188:191], v[116:119], v[234:237]
	v_mfma_f32_16x16x32_bf16 v[238:241], v[188:191], v[128:131], v[238:241]
	v_mfma_f32_16x16x32_bf16 v[160:163], v[192:195], v[116:119], v[160:163]
	v_mfma_f32_16x16x32_bf16 v[156:159], v[192:195], v[128:131], v[156:159]
	ds_read_b128 v[164:167], v181 offset:24576
	ds_read_b128 v[168:171], v181 offset:28672
	ds_read_b128 v[188:191], v182 offset:24576
	ds_read_b128 v[192:195], v182 offset:28672
	buffer_load_dwordx4 v185, s[40:43], s46 offen lds
	s_mov_b32 m0, s34
	s_waitcnt lgkmcnt(6)
	v_mfma_f32_16x16x32_bf16 v[8:11], v[132:135], v[120:123], v[36:39]
	v_mfma_f32_16x16x32_bf16 v[16:19], v[132:135], v[124:127], v[36:39]
	v_mfma_f32_16x16x32_bf16 v[152:155], v[136:139], v[120:123], v[36:39]
	v_mfma_f32_16x16x32_bf16 v[148:151], v[136:139], v[124:127], v[36:39]
	s_waitcnt lgkmcnt(4)
	v_mfma_f32_16x16x32_bf16 v[8:11], v[140:143], v[116:119], v[8:11]
	v_mfma_f32_16x16x32_bf16 v[16:19], v[140:143], v[128:131], v[16:19]
	v_mfma_f32_16x16x32_bf16 v[152:155], v[144:147], v[116:119], v[152:155]
	v_mfma_f32_16x16x32_bf16 v[148:151], v[144:147], v[128:131], v[148:151]
	buffer_load_dwordx4 v186, s[4:7], s54 offen lds
	s_mov_b32 m0, s35
	s_waitcnt lgkmcnt(2)
	v_mfma_f32_16x16x32_bf16 v[144:147], v[164:167], v[120:123], v[36:39]
	v_mfma_f32_16x16x32_bf16 v[140:143], v[164:167], v[124:127], v[36:39]
	v_mfma_f32_16x16x32_bf16 v[136:139], v[168:171], v[120:123], v[36:39]
	v_mfma_f32_16x16x32_bf16 v[132:135], v[168:171], v[124:127], v[36:39]
	buffer_load_dwordx4 v186, s[4:7], s55 offen lds
	s_waitcnt lgkmcnt(0)
	v_mfma_f32_16x16x32_bf16 v[144:147], v[188:191], v[116:119], v[144:147]
	v_mfma_f32_16x16x32_bf16 v[140:143], v[188:191], v[128:131], v[140:143]
	v_mfma_f32_16x16x32_bf16 v[136:139], v[192:195], v[116:119], v[136:139]
	v_mfma_f32_16x16x32_bf16 v[132:135], v[192:195], v[128:131], v[132:135]
	v_add_u32_e32 v187, 0x4000, v187
	v_add_u32_e32 v206, 0x4000, v206
	v_exp_f32_e32 v4, v12
	v_exp_f32_e32 v5, v13
	v_exp_f32_e32 v6, v14
	v_exp_f32_e32 v7, v15
	v_exp_f32_e32 v12, v222
	v_cvt_pk_fp8_f32 v4, v4, v5
	v_exp_f32_e32 v5, v223
	ds_read_b128 v[164:167], v187
	ds_read_b128 v[168:171], v206
	v_mfma_f32_16x16x128_f8f6f4 v[112:115], v[20:27], v[40:43], v[112:115] blgp:4
	v_cvt_pk_fp8_f32 v4, v6, v7 op_sel:[0,0,1]
	v_exp_f32_e32 v6, v224
	v_exp_f32_e32 v7, v225
	v_cvt_pk_fp8_f32 v12, v12, v5
	v_mfma_f32_16x16x128_f8f6f4 v[88:91], v[28:35], v[40:43], v[88:91] blgp:4
	ds_read_b128 v[188:191], v187 offset:2048
	ds_read_b128 v[192:195], v206 offset:2048
	s_waitcnt lgkmcnt(2)
	v_mfma_f32_16x16x128_f8f6f4 v[108:111], v[20:27], v[164:171], v[108:111]
	v_cvt_pk_fp8_f32 v12, v6, v7 op_sel:[0,0,1]
	v_exp_f32_e32 v5, v226
	v_exp_f32_e32 v6, v227
	v_exp_f32_e32 v13, v230
	v_mfma_f32_16x16x128_f8f6f4 v[80:83], v[28:35], v[164:171], v[80:83]
	v_exp_f32_e32 v15, v231
	v_exp_f32_e32 v7, v228
	v_exp_f32_e32 v14, v229
	v_cvt_pk_fp8_f32 v5, v5, v6
	v_exp_f32_e32 v6, v232
	v_exp_f32_e32 v207, v233
	v_cvt_pk_fp8_f32 v13, v13, v15
	ds_read_b128 v[164:167], v187 offset:4096
	ds_read_b128 v[168:171], v206 offset:4096
	v_cvt_pk_fp8_f32 v5, v7, v14 op_sel:[0,0,1]
	s_waitcnt lgkmcnt(2)
	v_mfma_f32_16x16x128_f8f6f4 v[104:107], v[20:27], v[188:195], v[104:107]
	v_cvt_pk_fp8_f32 v13, v6, v207 op_sel:[0,0,1]
	v_exp_f32_e32 v6, v234
	v_exp_f32_e32 v7, v235
	v_exp_f32_e32 v14, v238
	v_mfma_f32_16x16x128_f8f6f4 v[72:75], v[28:35], v[188:195], v[72:75]
	v_exp_f32_e32 v188, v239
	v_exp_f32_e32 v15, v236
	v_exp_f32_e32 v207, v237
	v_cvt_pk_fp8_f32 v6, v6, v7
	v_exp_f32_e32 v7, v240
	v_exp_f32_e32 v211, v241
	v_cvt_pk_fp8_f32 v14, v14, v188
	ds_read_b128 v[188:191], v187 offset:6144
	ds_read_b128 v[192:195], v206 offset:6144
	v_cvt_pk_fp8_f32 v6, v15, v207 op_sel:[0,0,1]
	s_waitcnt lgkmcnt(2)
	v_mfma_f32_16x16x128_f8f6f4 v[100:103], v[20:27], v[164:171], v[100:103]
	v_cvt_pk_fp8_f32 v14, v7, v211 op_sel:[0,0,1]
	v_exp_f32_e32 v7, v160
	v_exp_f32_e32 v160, v161
	v_exp_f32_e32 v15, v156
	v_mfma_f32_16x16x128_f8f6f4 v[64:67], v[28:35], v[164:171], v[64:67]
	v_exp_f32_e32 v156, v157
	v_exp_f32_e32 v164, v162
	v_exp_f32_e32 v165, v163
	v_cvt_pk_fp8_f32 v7, v7, v160
	v_exp_f32_e32 v166, v158
	v_exp_f32_e32 v167, v159
	v_cvt_pk_fp8_f32 v15, v15, v156
	ds_read_b128 v[156:159], v187 offset:8192
	ds_read_b128 v[160:163], v206 offset:8192
	v_cvt_pk_fp8_f32 v7, v164, v165 op_sel:[0,0,1]
	s_waitcnt lgkmcnt(2)
	v_mfma_f32_16x16x128_f8f6f4 v[96:99], v[20:27], v[188:195], v[96:99]
	v_cvt_pk_fp8_f32 v15, v166, v167 op_sel:[0,0,1]
	v_exp_f32_e32 v8, v8
	v_exp_f32_e32 v9, v9
	v_exp_f32_e32 v16, v16
	v_mfma_f32_16x16x128_f8f6f4 v[60:63], v[28:35], v[188:195], v[60:63]
	v_exp_f32_e32 v17, v17
	v_exp_f32_e32 v10, v10
	v_exp_f32_e32 v11, v11
	v_cvt_pk_fp8_f32 v8, v8, v9
	v_exp_f32_e32 v9, v18
	v_exp_f32_e32 v18, v19
	v_cvt_pk_fp8_f32 v16, v16, v17
	ds_read_b128 v[164:167], v187 offset:10240
	ds_read_b128 v[168:171], v206 offset:10240
	v_cvt_pk_fp8_f32 v8, v10, v11 op_sel:[0,0,1]
	s_waitcnt lgkmcnt(2)
	v_mfma_f32_16x16x128_f8f6f4 v[92:95], v[20:27], v[156:163], v[92:95]
	v_cvt_pk_fp8_f32 v16, v9, v18 op_sel:[0,0,1]
	v_exp_f32_e32 v9, v152
	v_exp_f32_e32 v10, v153
	v_exp_f32_e32 v17, v148
	v_mfma_f32_16x16x128_f8f6f4 v[56:59], v[28:35], v[156:163], v[56:59]
	v_exp_f32_e32 v19, v149
	v_exp_f32_e32 v11, v154
	v_exp_f32_e32 v18, v155
	v_cvt_pk_fp8_f32 v9, v9, v10
	v_exp_f32_e32 v10, v150
	v_exp_f32_e32 v156, v151
	v_cvt_pk_fp8_f32 v17, v17, v19
	ds_read_b128 v[148:151], v187 offset:12288
	ds_read_b128 v[152:155], v206 offset:12288
	v_cvt_pk_fp8_f32 v9, v11, v18 op_sel:[0,0,1]
	s_waitcnt lgkmcnt(2)
	v_mfma_f32_16x16x128_f8f6f4 v[84:87], v[20:27], v[164:171], v[84:87]
	v_cvt_pk_fp8_f32 v17, v10, v156 op_sel:[0,0,1]
	v_exp_f32_e32 v10, v144
	v_exp_f32_e32 v11, v145
	v_exp_f32_e32 v18, v140
	v_mfma_f32_16x16x128_f8f6f4 v[52:55], v[28:35], v[164:171], v[52:55]
	v_exp_f32_e32 v140, v141
	v_exp_f32_e32 v19, v146
	v_exp_f32_e32 v156, v147
	v_cvt_pk_fp8_f32 v10, v10, v11
	v_exp_f32_e32 v11, v142
	v_exp_f32_e32 v157, v143
	v_cvt_pk_fp8_f32 v18, v18, v140
	ds_read_b128 v[140:143], v187 offset:14336
	ds_read_b128 v[144:147], v206 offset:14336
	v_cvt_pk_fp8_f32 v10, v19, v156 op_sel:[0,0,1]
	s_waitcnt lgkmcnt(2)
	v_mfma_f32_16x16x128_f8f6f4 v[76:79], v[20:27], v[148:155], v[76:79]
	v_cvt_pk_fp8_f32 v18, v11, v157 op_sel:[0,0,1]
	v_exp_f32_e32 v11, v136
	v_exp_f32_e32 v19, v137
	v_mfma_f32_16x16x128_f8f6f4 v[48:51], v[28:35], v[148:155], v[48:51]
	s_waitcnt lgkmcnt(0)
	v_mfma_f32_16x16x128_f8f6f4 v[68:71], v[20:27], v[140:147], v[68:71]
	v_exp_f32_e32 v20, v138
	v_exp_f32_e32 v21, v139
	v_cvt_pk_fp8_f32 v11, v11, v19
	v_exp_f32_e32 v19, v132
	v_exp_f32_e32 v22, v135
	v_mfma_f32_16x16x128_f8f6f4 v[44:47], v[28:35], v[140:147], v[44:47]
	v_cvt_pk_fp8_f32 v11, v20, v21 op_sel:[0,0,1]
	v_exp_f32_e32 v20, v133
	v_exp_f32_e32 v21, v134
	v_cvt_pk_fp8_f32 v19, v19, v20
	v_cvt_pk_fp8_f32 v19, v21, v22 op_sel:[0,0,1]
	s_add_i32 s44, s44, 0x300000
	s_add_i32 s47, s47, 0x8000
	s_add_i32 s46, s46, 0x8000
	s_xor_b32 s53, s53, 0x8000
	s_xor_b32 s51, s51, 0xffff0000
	s_add_i32 s37, s37, 2
	s_cmpk_lt_u32 s37, 0x80
	s_cbranch_scc1 .LBB0_374
	s_waitcnt vmcnt(0)
	s_barrier
	ds_read_b128 v[20:23], v181 offset:32768
	ds_read_b128 v[24:27], v182 offset:32768
	s_waitcnt lgkmcnt(1)
	v_mfma_f32_16x16x32_bf16 v[28:31], v[20:23], v[120:123], v[36:39]
	v_mfma_f32_16x16x32_bf16 v[20:23], v[20:23], v[124:127], v[36:39]
	s_waitcnt lgkmcnt(0)
	v_mfma_f32_16x16x32_bf16 v[144:147], v[24:27], v[116:119], v[28:31]
	v_mfma_f32_16x16x32_bf16 v[20:23], v[24:27], v[128:131], v[20:23]
	ds_read_b128 v[24:27], v181 offset:36864
	s_nop 2
	ds_read_b128 v[28:31], v182 offset:36864
	s_waitcnt lgkmcnt(1)
	v_mfma_f32_16x16x32_bf16 v[32:35], v[24:27], v[120:123], v[36:39]
	v_mfma_f32_16x16x32_bf16 v[24:27], v[24:27], v[124:127], v[36:39]
	s_waitcnt lgkmcnt(0)
	v_mfma_f32_16x16x32_bf16 v[152:155], v[28:31], v[116:119], v[32:35]
	v_mfma_f32_16x16x32_bf16 v[28:31], v[28:31], v[128:131], v[24:27]
	s_nop 4
	ds_read_b128 v[24:27], v181 offset:40960
	ds_read_b128 v[32:35], v182 offset:40960
	s_waitcnt lgkmcnt(1)
	v_mfma_f32_16x16x32_bf16 v[132:135], v[24:27], v[120:123], v[36:39]
	v_mfma_f32_16x16x32_bf16 v[24:27], v[24:27], v[124:127], v[36:39]
	s_waitcnt lgkmcnt(0)
	v_mfma_f32_16x16x32_bf16 v[148:151], v[32:35], v[116:119], v[132:135]
	v_mfma_f32_16x16x32_bf16 v[24:27], v[32:35], v[128:131], v[24:27]
	ds_read_b128 v[32:35], v181 offset:45056
	s_nop 2
	ds_read_b128 v[132:135], v182 offset:45056
	s_waitcnt lgkmcnt(1)
	v_mfma_f32_16x16x32_bf16 v[136:139], v[32:35], v[120:123], v[36:39]
	v_mfma_f32_16x16x32_bf16 v[32:35], v[32:35], v[124:127], v[36:39]
	s_waitcnt lgkmcnt(0)
	v_mfma_f32_16x16x32_bf16 v[160:163], v[132:135], v[116:119], v[136:139]
	v_mfma_f32_16x16x32_bf16 v[132:135], v[132:135], v[128:131], v[32:35]
	s_nop 4
	ds_read_b128 v[32:35], v181 offset:49152
	ds_read_b128 v[136:139], v182 offset:49152
	s_waitcnt lgkmcnt(1)
	v_mfma_f32_16x16x32_bf16 v[140:143], v[32:35], v[120:123], v[36:39]
	v_mfma_f32_16x16x32_bf16 v[32:35], v[32:35], v[124:127], v[36:39]
	s_waitcnt lgkmcnt(0)
	v_mfma_f32_16x16x32_bf16 v[156:159], v[136:139], v[116:119], v[140:143]
	v_mfma_f32_16x16x32_bf16 v[32:35], v[136:139], v[128:131], v[32:35]
	ds_read_b128 v[136:139], v181 offset:53248
	s_nop 2
	ds_read_b128 v[140:143], v182 offset:53248
	s_waitcnt lgkmcnt(1)
	v_mfma_f32_16x16x32_bf16 v[164:167], v[136:139], v[120:123], v[36:39]
	v_mfma_f32_16x16x32_bf16 v[136:139], v[136:139], v[124:127], v[36:39]
	s_waitcnt lgkmcnt(0)
	v_mfma_f32_16x16x32_bf16 v[168:171], v[140:143], v[116:119], v[164:167]
	v_mfma_f32_16x16x32_bf16 v[140:143], v[140:143], v[128:131], v[136:139]
	s_nop 4
	ds_read_b128 v[136:139], v181 offset:57344
	ds_read_b128 v[184:187], v182 offset:57344
	s_waitcnt lgkmcnt(1)
	v_mfma_f32_16x16x32_bf16 v[164:167], v[136:139], v[120:123], v[36:39]
	v_mfma_f32_16x16x32_bf16 v[136:139], v[136:139], v[124:127], v[36:39]
	s_waitcnt lgkmcnt(0)
	v_mfma_f32_16x16x32_bf16 v[164:167], v[184:187], v[116:119], v[164:167]
	v_mfma_f32_16x16x32_bf16 v[136:139], v[184:187], v[128:131], v[136:139]
	ds_read_b128 v[184:187], v181 offset:61440
	ds_read_b128 v[188:191], v182 offset:61440
	s_waitcnt lgkmcnt(1)
	v_mfma_f32_16x16x32_bf16 v[120:123], v[184:187], v[120:123], v[36:39]
	s_waitcnt lgkmcnt(0)
	v_mfma_f32_16x16x32_bf16 v[116:119], v[188:191], v[116:119], v[120:123]
	v_mfma_f32_16x16x32_bf16 v[120:123], v[184:187], v[124:127], v[36:39]
	v_mfma_f32_16x16x32_bf16 v[128:131], v[188:191], v[128:131], v[120:123]
	s_nop 6
	v_add_u32_e32 v120, 0x18000, v180
	v_add_u32_e32 v181, v120, v178
	v_add_u32_e32 v190, v120, v179
	ds_read_b128 v[120:123], v181
	ds_read_b128 v[124:127], v190
	v_mfma_f32_16x16x128_f8f6f4 v[112:115], v[4:11], v[40:43], v[112:115] blgp:4
	v_mfma_f32_16x16x128_f8f6f4 v[88:91], v[12:19], v[40:43], v[88:91] blgp:4
	ds_read_b128 v[182:185], v181 offset:2048
	ds_read_b128 v[186:189], v190 offset:2048
	s_waitcnt lgkmcnt(2)
	v_mfma_f32_16x16x128_f8f6f4 v[108:111], v[4:11], v[120:127], v[108:111]
	v_mfma_f32_16x16x128_f8f6f4 v[80:83], v[12:19], v[120:127], v[80:83]
	ds_read_b128 v[120:123], v181 offset:4096
	ds_read_b128 v[124:127], v190 offset:4096
	s_waitcnt lgkmcnt(2)
	v_mfma_f32_16x16x128_f8f6f4 v[104:107], v[4:11], v[182:189], v[104:107]
	v_mfma_f32_16x16x128_f8f6f4 v[72:75], v[12:19], v[182:189], v[72:75]
	ds_read_b128 v[182:185], v181 offset:6144
	ds_read_b128 v[186:189], v190 offset:6144
	s_waitcnt lgkmcnt(2)
	v_mfma_f32_16x16x128_f8f6f4 v[100:103], v[4:11], v[120:127], v[100:103]
	v_mfma_f32_16x16x128_f8f6f4 v[64:67], v[12:19], v[120:127], v[64:67]
	ds_read_b128 v[120:123], v181 offset:8192
	ds_read_b128 v[124:127], v190 offset:8192
	s_waitcnt lgkmcnt(2)
	v_mfma_f32_16x16x128_f8f6f4 v[96:99], v[4:11], v[182:189], v[96:99]
	v_mfma_f32_16x16x128_f8f6f4 v[60:63], v[12:19], v[182:189], v[60:63]
	ds_read_b128 v[182:185], v181 offset:10240
	ds_read_b128 v[186:189], v190 offset:10240
	s_waitcnt lgkmcnt(2)
	v_mfma_f32_16x16x128_f8f6f4 v[92:95], v[4:11], v[120:127], v[92:95]
	v_mfma_f32_16x16x128_f8f6f4 v[56:59], v[12:19], v[120:127], v[56:59]
	ds_read_b128 v[120:123], v181 offset:12288
	ds_read_b128 v[124:127], v190 offset:12288
	s_waitcnt lgkmcnt(2)
	v_mfma_f32_16x16x128_f8f6f4 v[84:87], v[4:11], v[182:189], v[84:87]
	v_mfma_f32_16x16x128_f8f6f4 v[52:55], v[12:19], v[182:189], v[52:55]
	ds_read_b128 v[182:185], v181 offset:14336
	ds_read_b128 v[186:189], v190 offset:14336
	s_waitcnt lgkmcnt(2)
	v_mfma_f32_16x16x128_f8f6f4 v[76:79], v[4:11], v[120:127], v[76:79]
	v_mfma_f32_16x16x128_f8f6f4 v[48:51], v[12:19], v[120:127], v[48:51]
	s_waitcnt lgkmcnt(0)
	v_mfma_f32_16x16x128_f8f6f4 v[68:71], v[4:11], v[182:189], v[68:71]
	v_mfma_f32_16x16x128_f8f6f4 v[44:47], v[12:19], v[182:189], v[44:47]
	v_exp_f32_e32 v11, v128
	v_exp_f32_e32 v5, v129
	v_exp_f32_e32 v12, v144
	v_exp_f32_e32 v7, v145
	v_exp_f32_e32 v13, v152
	v_exp_f32_e32 v9, v153
	v_exp_f32_e32 v14, v148
	v_exp_f32_e32 v15, v149
	v_cvt_pk_fp8_f32 v11, v11, v5
	v_exp_f32_e32 v5, v146
	v_exp_f32_e32 v8, v147
	v_cvt_pk_fp8_f32 v12, v12, v7
	v_exp_f32_e32 v7, v154
	v_exp_f32_e32 v10, v155
	v_cvt_pk_fp8_f32 v13, v13, v9
	v_exp_f32_e32 v9, v150
	v_exp_f32_e32 v16, v151
	v_cvt_pk_fp8_f32 v14, v14, v15
	v_exp_f32_e32 v4, v130
	v_exp_f32_e32 v6, v131
	v_cvt_pk_fp8_f32 v12, v5, v8 op_sel:[0,0,1]
	v_cvt_pk_fp8_f32 v13, v7, v10 op_sel:[0,0,1]
	v_cvt_pk_fp8_f32 v14, v9, v16 op_sel:[0,0,1]
	v_exp_f32_e32 v15, v160
	v_exp_f32_e32 v5, v161
	v_exp_f32_e32 v16, v156
	v_exp_f32_e32 v7, v157
	v_cvt_pk_fp8_f32 v11, v4, v6 op_sel:[0,0,1]
	v_exp_f32_e32 v4, v162
	v_exp_f32_e32 v6, v163
	v_cvt_pk_fp8_f32 v15, v15, v5
	v_exp_f32_e32 v5, v158
	v_exp_f32_e32 v8, v159
	v_cvt_pk_fp8_f32 v16, v16, v7
	v_exp_f32_e32 v17, v168
	v_exp_f32_e32 v9, v169
	v_exp_f32_e32 v18, v164
	v_exp_f32_e32 v19, v165
	v_exp_f32_e32 v7, v170
	v_exp_f32_e32 v10, v171
	v_cvt_pk_fp8_f32 v17, v17, v9
	v_exp_f32_e32 v9, v166
	v_exp_f32_e32 v120, v167
	v_cvt_pk_fp8_f32 v18, v18, v19
	v_cvt_pk_fp8_f32 v15, v4, v6 op_sel:[0,0,1]
	v_cvt_pk_fp8_f32 v16, v5, v8 op_sel:[0,0,1]
	v_exp_f32_e32 v19, v116
	v_exp_f32_e32 v5, v117
	v_exp_f32_e32 v4, v20
	v_exp_f32_e32 v6, v21
	v_cvt_pk_fp8_f32 v17, v7, v10 op_sel:[0,0,1]
	v_cvt_pk_fp8_f32 v18, v9, v120 op_sel:[0,0,1]
	v_exp_f32_e32 v7, v118
	v_exp_f32_e32 v8, v119
	v_cvt_pk_fp8_f32 v19, v19, v5
	v_exp_f32_e32 v9, v22
	v_exp_f32_e32 v10, v23
	v_cvt_pk_fp8_f32 v4, v4, v6
	v_exp_f32_e32 v5, v28
	v_exp_f32_e32 v21, v29
	v_exp_f32_e32 v6, v24
	v_exp_f32_e32 v23, v25
	v_cvt_pk_fp8_f32 v19, v7, v8 op_sel:[0,0,1]
	v_cvt_pk_fp8_f32 v4, v9, v10 op_sel:[0,0,1]
	v_exp_f32_e32 v7, v132
	v_exp_f32_e32 v9, v133
	v_exp_f32_e32 v8, v32
	v_exp_f32_e32 v10, v33
	v_exp_f32_e32 v20, v30
	v_exp_f32_e32 v22, v31
	v_cvt_pk_fp8_f32 v5, v5, v21
	v_exp_f32_e32 v21, v26
	v_exp_f32_e32 v24, v27
	v_cvt_pk_fp8_f32 v6, v6, v23
	v_cvt_pk_fp8_f32 v7, v7, v9
	v_cvt_pk_fp8_f32 v8, v8, v10
	v_exp_f32_e32 v9, v140
	v_exp_f32_e32 v25, v141
	v_exp_f32_e32 v10, v136
	v_exp_f32_e32 v27, v137
	v_cvt_pk_fp8_f32 v5, v20, v22 op_sel:[0,0,1]
	v_cvt_pk_fp8_f32 v6, v21, v24 op_sel:[0,0,1]
	v_exp_f32_e32 v20, v134
	v_exp_f32_e32 v21, v135
	v_cvt_pk_fp8_f32 v9, v9, v25
	v_exp_f32_e32 v25, v138
	v_exp_f32_e32 v28, v139
	v_cvt_pk_fp8_f32 v10, v10, v27
	v_exp_f32_e32 v22, v34
	v_exp_f32_e32 v23, v35
	v_exp_f32_e32 v24, v142
	v_exp_f32_e32 v26, v143
	v_cvt_pk_fp8_f32 v7, v20, v21 op_sel:[0,0,1]
	v_add_u32_e32 v20, 0x1c000, v180
	v_cvt_pk_fp8_f32 v10, v25, v28 op_sel:[0,0,1]
	v_add_u32_e32 v28, v20, v178
	v_cvt_pk_fp8_f32 v8, v22, v23 op_sel:[0,0,1]
	v_cvt_pk_fp8_f32 v9, v24, v26 op_sel:[0,0,1]
	s_nop 1
	v_mfma_f32_16x16x128_f8f6f4 v[112:115], v[12:19], v[40:43], v[112:115] blgp:4
	v_add_u32_e32 v29, v20, v179
	v_mfma_f32_16x16x128_f8f6f4 v[88:91], v[4:11], v[40:43], v[88:91] blgp:4
	ds_read_b128 v[20:23], v28
	ds_read_b128 v[24:27], v29
	s_waitcnt lgkmcnt(0)
	v_mfma_f32_16x16x128_f8f6f4 v[108:111], v[12:19], v[20:27], v[108:111]
	v_mfma_f32_16x16x128_f8f6f4 v[80:83], v[4:11], v[20:27], v[80:83]
	ds_read_b128 v[20:23], v28 offset:2048
	ds_read_b128 v[24:27], v29 offset:2048
	s_waitcnt lgkmcnt(0)
	v_mfma_f32_16x16x128_f8f6f4 v[104:107], v[12:19], v[20:27], v[104:107]
	v_mfma_f32_16x16x128_f8f6f4 v[72:75], v[4:11], v[20:27], v[72:75]
	ds_read_b128 v[20:23], v28 offset:4096
	ds_read_b128 v[24:27], v29 offset:4096
	s_waitcnt lgkmcnt(0)
	v_mfma_f32_16x16x128_f8f6f4 v[100:103], v[12:19], v[20:27], v[100:103]
	v_mfma_f32_16x16x128_f8f6f4 v[64:67], v[4:11], v[20:27], v[64:67]
	ds_read_b128 v[20:23], v28 offset:6144
	ds_read_b128 v[24:27], v29 offset:6144
	s_waitcnt lgkmcnt(0)
	v_mfma_f32_16x16x128_f8f6f4 v[96:99], v[12:19], v[20:27], v[96:99]
	v_mfma_f32_16x16x128_f8f6f4 v[60:63], v[4:11], v[20:27], v[60:63]
	ds_read_b128 v[20:23], v28 offset:8192
	ds_read_b128 v[24:27], v29 offset:8192
	s_waitcnt lgkmcnt(0)
	v_mfma_f32_16x16x128_f8f6f4 v[92:95], v[12:19], v[20:27], v[92:95]
	v_mfma_f32_16x16x128_f8f6f4 v[56:59], v[4:11], v[20:27], v[56:59]
	ds_read_b128 v[20:23], v28 offset:10240
	ds_read_b128 v[24:27], v29 offset:10240
	s_waitcnt lgkmcnt(0)
	v_mfma_f32_16x16x128_f8f6f4 v[84:87], v[12:19], v[20:27], v[84:87]
	v_mfma_f32_16x16x128_f8f6f4 v[52:55], v[4:11], v[20:27], v[52:55]
	ds_read_b128 v[20:23], v28 offset:12288
	ds_read_b128 v[24:27], v29 offset:12288
	s_waitcnt lgkmcnt(0)
	v_mfma_f32_16x16x128_f8f6f4 v[76:79], v[12:19], v[20:27], v[76:79]
	v_mfma_f32_16x16x128_f8f6f4 v[48:51], v[4:11], v[20:27], v[48:51]
	ds_read_b128 v[20:23], v28 offset:14336
	ds_read_b128 v[24:27], v29 offset:14336
	s_waitcnt lgkmcnt(0)
	v_mfma_f32_16x16x128_f8f6f4 v[68:71], v[12:19], v[20:27], v[68:71]
	v_mfma_f32_16x16x128_f8f6f4 v[44:47], v[4:11], v[20:27], v[44:47]
	v_rcp_f32_e32 v4, v112
	v_rcp_f32_e32 v6, v113
	s_nop 15
	s_nop 15
	v_readlane_b32 s4, v253, 16
	v_mul_f32_e32 v8, v4, v108
	v_mul_f32_e32 v10, v4, v104
	v_mul_f32_e32 v12, v4, v100
	v_mul_f32_e32 v14, v4, v96
	v_mul_f32_e32 v16, v4, v92
	v_mul_f32_e32 v18, v4, v84
	v_mul_f32_e32 v20, v4, v76
	v_mul_f32_e32 v5, v4, v68
	v_mul_f32_e32 v118, v6, v109
	v_mul_f32_e32 v119, v6, v105
	v_mul_f32_e32 v117, v6, v101
	v_mul_f32_e32 v116, v6, v97
	v_mul_f32_e32 v112, v6, v93
	v_rcp_f32_e32 v4, v114
	v_mul_f32_e32 v114, v6, v85
	v_mul_f32_e32 v113, v6, v77
	v_mul_f32_e32 v109, v6, v69
	v_rcp_f32_e32 v6, v115
	v_mul_f32_e32 v108, v4, v110
	v_mul_f32_e32 v105, v4, v106
	v_mul_f32_e32 v104, v4, v102
	v_mul_f32_e32 v102, v4, v98
	v_mul_f32_e32 v101, v4, v94
	v_mul_f32_e32 v100, v4, v86
	v_mul_f32_e32 v98, v4, v78
	v_mul_f32_e32 v97, v4, v70
	v_mul_f32_e32 v94, v6, v111
	v_mul_f32_e32 v96, v6, v107
	v_mul_f32_e32 v93, v6, v103
	v_mul_f32_e32 v92, v6, v99
	v_mul_f32_e32 v86, v6, v95
	v_rcp_f32_e32 v4, v88
	v_mul_f32_e32 v88, v6, v87
	v_mul_f32_e32 v87, v6, v79
	v_mul_f32_e32 v85, v6, v71
	v_rcp_f32_e32 v6, v89
	v_mul_f32_e32 v84, v4, v80
	v_mul_f32_e32 v80, v4, v72
	v_mul_f32_e32 v79, v4, v64
	v_mul_f32_e32 v78, v4, v60
	v_mul_f32_e32 v77, v4, v56
	v_mul_f32_e32 v23, v4, v52
	v_mul_f32_e32 v22, v4, v48
	v_mul_f32_e32 v76, v4, v44
	v_mul_f32_e32 v72, v6, v81
	v_mul_f32_e32 v73, v6, v73
	v_mul_f32_e32 v71, v6, v65
	v_mul_f32_e32 v69, v6, v61
	v_mul_f32_e32 v65, v6, v57
	v_rcp_f32_e32 v4, v90
	v_mul_f32_e32 v70, v6, v53
	v_mul_f32_e32 v68, v6, v49
	v_mul_f32_e32 v64, v6, v45
	v_rcp_f32_e32 v6, v91
	v_readlane_b32 s5, v253, 17
	v_mul_f32_e32 v61, v4, v82
	v_mul_f32_e32 v60, v4, v74
	v_mul_f32_e32 v57, v4, v66
	v_mul_f32_e32 v56, v4, v62
	v_mul_f32_e32 v53, v4, v58
	v_mul_f32_e32 v52, v4, v54
	v_mul_f32_e32 v49, v4, v50
	v_mul_f32_e32 v48, v4, v46
	v_mul_f32_e32 v42, v6, v83
	v_mul_f32_e32 v43, v6, v75
	v_mul_f32_e32 v41, v6, v67
	v_mul_f32_e32 v40, v6, v63
	v_mul_f32_e32 v34, v6, v59
	v_mul_f32_e32 v33, v6, v55
	v_mul_f32_e32 v32, v6, v51
	s_andn2_b64 vcc, exec, s[4:5]
	v_mul_f32_e32 v35, v6, v47
	s_waitcnt vmcnt(0)
	s_barrier
	s_cbranch_vccnz .LBB0_377
	v_add_u32_e32 v4, s84, v2
	v_lshl_add_u32 v4, v4, 2, 0
	ds_write2st64_b32 v4, v8, v118 offset1:4
	ds_write2st64_b32 v4, v108, v94 offset0:8 offset1:12
	ds_write2st64_b32 v4, v10, v119 offset0:16 offset1:20
	ds_write2st64_b32 v4, v105, v96 offset0:24 offset1:28
	ds_write2st64_b32 v4, v12, v117 offset0:32 offset1:36
	ds_write2st64_b32 v4, v104, v93 offset0:40 offset1:44
	ds_write2st64_b32 v4, v14, v116 offset0:48 offset1:52
	ds_write2st64_b32 v4, v102, v92 offset0:56 offset1:60
	ds_write2st64_b32 v4, v16, v112 offset0:64 offset1:68
	ds_write2st64_b32 v4, v101, v86 offset0:72 offset1:76
	ds_write2st64_b32 v4, v18, v114 offset0:80 offset1:84
	ds_write2st64_b32 v4, v100, v88 offset0:88 offset1:92
	ds_write2st64_b32 v4, v20, v113 offset0:96 offset1:100
	ds_write2st64_b32 v4, v98, v87 offset0:104 offset1:108
	ds_write2st64_b32 v4, v5, v109 offset0:112 offset1:116
	ds_write2st64_b32 v4, v97, v85 offset0:120 offset1:124
	ds_write2st64_b32 v4, v84, v72 offset0:128 offset1:132
	ds_write2st64_b32 v4, v61, v42 offset0:136 offset1:140
	ds_write2st64_b32 v4, v80, v73 offset0:144 offset1:148
	ds_write2st64_b32 v4, v60, v43 offset0:152 offset1:156
	ds_write2st64_b32 v4, v79, v71 offset0:160 offset1:164
	ds_write2st64_b32 v4, v57, v41 offset0:168 offset1:172
	ds_write2st64_b32 v4, v78, v69 offset0:176 offset1:180
	ds_write2st64_b32 v4, v56, v40 offset0:184 offset1:188
	ds_write2st64_b32 v4, v77, v65 offset0:192 offset1:196
	ds_write2st64_b32 v4, v53, v34 offset0:200 offset1:204
	ds_write2st64_b32 v4, v23, v70 offset0:208 offset1:212
	ds_write2st64_b32 v4, v52, v33 offset0:216 offset1:220
	ds_write2st64_b32 v4, v22, v68 offset0:224 offset1:228
	ds_write2st64_b32 v4, v49, v32 offset0:232 offset1:236
	ds_write2st64_b32 v4, v76, v64 offset0:240 offset1:244
	ds_write2st64_b32 v4, v48, v35 offset0:248 offset1:252
